# s14p + phase-2 conversion: the 16 per-row folded-norm gain loads of bf16 PLE-gate tiles issued up front instead of load+vmcnt(0) per row; padded
# speedup vs baseline: 1.0045x; 1.0045x over previous
; #define LAS __attribute__((address_space(3)))
; DI unsigned pk2(float lo, float hi) { const f32x2 v = {lo, hi}; return __builtin_bit_cast(unsigned, __builtin_convertvector(v, bf16x2_t)); }
; template <bool F8> DI void tr_tile(const float* __restrict__ W, int ldn, int K, int k0, int nsrc0, unsigned char* __restrict__ WT, int ndst0, LAS unsigned char* scr, int lane, float wscale, const float* gk = nullptr  ) {
;     ...
;     for (int i = 0; i < 16; ++i) v[i] = __builtin_nontemporal_load((const f32x4*)(W + (size_t)(k0 + 4 * i + r) * ldn + nsrc0 + 4 * c4));
; #pragma unroll
;     for (int i = 0; i < 16; ++i) { f32x4 x = F8 ? v[i] * wscale : v[i]; if (!F8 && gk) x = x * gk[k0 + 4 * i + r];
;         *(LAS unsigned long long*)(scr + (4 * i + r) * 144 + c4 * 8) = (unsigned long long)pk2(x[0], x[1]) | ((unsigned long long)pk2(x[2], x[3]) << 32); }
; template <int PART> DI void prologue_phase(const Params& P, const Frame& F) {
;     ...
;         const int kb = r / ntn, nb = r % ntn, k0 = 64 * kb, ndst0 = 64 * nb;
;         int nsrc0 = ndst0;
;         if (kind == 1) nsrc0 = ndst0 + (ndst0 >= 3072 ? 8 : 0);
;         if (kind == 2) { const int t = nb >> 2, q = nb & 3; if (q >= 2) src = src2; nsrc0 = 128 * t + 64 * (q & 1); }
.LBB0_180:
	s_sext_i32_i16 s13, s0
	v_cvt_f32_i32_e32 v0, s13
	s_cmp_gt_u32 s57, 0x179ff
	s_sext_i32_i16 s57, s58
	v_cvt_f32_i32_e32 v1, s57
	v_rcp_iflag_f32_e32 v2, v0
	s_cselect_b64 s[24:25], -1, 0
	s_cmpk_gt_u32 s56, 0x3ff
	s_cselect_b64 s[60:61], -1, 0
	v_mul_f32_e32 v2, v1, v2
	v_trunc_f32_e32 v2, v2
	s_xor_b32 s13, s57, s13
	v_fma_f32 v1, -v2, v0, v1
	v_cvt_i32_f32_e32 v2, v2
	s_ashr_i32 s13, s13, 30
	s_and_b64 s[24:25], s[24:25], s[60:61]
	s_or_b32 s13, s13, 1
	v_cmp_ge_f32_e64 s[60:61], |v1|, |v0|
	s_and_b64 s[60:61], s[60:61], exec
	s_cselect_b32 s13, s13, 0
	v_readfirstlane_b32 s57, v2
	s_add_i32 s13, s57, s13
	s_sext_i32_i16 s57, s13
	s_mul_i32 s13, s13, s0
	s_sub_i32 s60, s58, s13
	s_sext_i32_i16 s61, s60
	s_lshl_b32 s0, s57, 6
	s_lshl_b32 s13, s61, 6
	s_cmp_gt_i32 s61, 47
	s_cselect_b64 s[58:59], -1, 0
	s_and_b64 s[4:5], s[4:5], s[58:59]
	s_and_b64 s[4:5], s[4:5], exec
	s_cselect_b32 s4, 8, 0
	s_or_b32 s57, s4, s13
	s_bitcmp0_b32 s60, 1
	s_cselect_b32 s58, s22, s20
	s_cselect_b32 s21, s23, s21
	s_lshl_b32 s4, s61, 5
	s_and_b32 s4, s4, 0xffffff80
	s_and_b32 s5, s13, 64
	s_or_b32 s20, s4, s5
	s_and_b64 s[4:5], s[18:19], exec
	v_add_u32_e32 v70, s0, v75
	s_cselect_b32 s20, s20, s57
	s_cselect_b32 s23, s21, s23
	s_cselect_b32 s22, s58, s22
	s_mov_b64 s[4:5], -1
	s_and_b64 vcc, exec, s[24:25]
	v_ashrrev_i32_e32 v71, 31, v70
	v_mul_lo_u32 v106, s17, v70
	v_add_u32_e32 v105, 4, v70
	v_add_u32_e32 v104, 8, v70
	v_add_u32_e32 v103, 12, v70
	v_add_u32_e32 v102, 16, v70
	v_add_u32_e32 v101, 20, v70
	v_add_u32_e32 v100, 24, v70
	v_add_u32_e32 v99, 28, v70
	v_add_u32_e32 v98, 32, v70
	v_add_u32_e32 v97, 36, v70
	v_add_u32_e32 v96, 40, v70
	v_add_u32_e32 v95, 44, v70
	v_add_u32_e32 v94, 48, v70
	v_add_u32_e32 v93, 52, v70
	v_add_u32_e32 v92, 56, v70
	v_add_u32_e32 v91, 60, v70
	s_cbranch_vccz .LBB0_214
	s_cmp_lt_u32 s56, 0xfffffc00
	s_cselect_b64 s[4:5], -1, 0
	s_or_b64 vcc, s[4:5], s[10:11]
	s_cbranch_vccnz .Lpg_nogain
	v_lshl_add_u64 v[72:73], v[70:71], 2, s[44:45]
	global_load_dword v206, v[72:73], off
	global_load_dword v207, v[72:73], off offset:16
	global_load_dword v208, v[72:73], off offset:32
	global_load_dword v209, v[72:73], off offset:48
	global_load_dword v210, v[72:73], off offset:64
	global_load_dword v211, v[72:73], off offset:80
	global_load_dword v212, v[72:73], off offset:96
	global_load_dword v213, v[72:73], off offset:112
	global_load_dword v214, v[72:73], off offset:128
	global_load_dword v215, v[72:73], off offset:144
	global_load_dword v216, v[72:73], off offset:160
	global_load_dword v217, v[72:73], off offset:176
	global_load_dword v218, v[72:73], off offset:192
	global_load_dword v219, v[72:73], off offset:208
	global_load_dword v220, v[72:73], off offset:224
	global_load_dword v221, v[72:73], off offset:240
.Lpg_nogain:
	s_ashr_i32 s21, s20, 31
	s_lshl_b64 s[24:25], s[20:21], 2
	s_add_u32 s24, s22, s24
	s_addc_u32 s25, s23, s25
	v_lshl_add_u64 v[0:1], s[24:25], 0, v[64:65]
	v_mul_lo_u32 v4, s16, v71
	v_mad_u64_u32 v[2:3], s[24:25], s16, v70, 0
	v_add3_u32 v3, v3, v4, v106
	v_ashrrev_i32_e32 v4, 31, v105
	v_mul_lo_u32 v6, s16, v4
	v_mul_lo_u32 v7, s17, v105
	v_mad_u64_u32 v[4:5], s[24:25], s16, v105, 0
	v_lshl_add_u64 v[2:3], v[2:3], 2, v[0:1]
	v_add3_u32 v5, v5, v6, v7
	v_lshl_add_u64 v[4:5], v[4:5], 2, v[0:1]
	global_load_dwordx4 v[60:63], v[2:3], off nt
	global_load_dwordx4 v[56:59], v[4:5], off nt
	v_ashrrev_i32_e32 v2, 31, v104
	v_mul_lo_u32 v4, s16, v2
	v_mul_lo_u32 v5, s17, v104
	v_mad_u64_u32 v[2:3], s[24:25], s16, v104, 0
	v_add3_u32 v3, v3, v4, v5
	v_ashrrev_i32_e32 v4, 31, v103
	v_mul_lo_u32 v6, s16, v4
	v_mul_lo_u32 v7, s17, v103
	v_mad_u64_u32 v[4:5], s[24:25], s16, v103, 0
	v_lshl_add_u64 v[2:3], v[2:3], 2, v[0:1]
	v_add3_u32 v5, v5, v6, v7
	v_lshl_add_u64 v[4:5], v[4:5], 2, v[0:1]
	global_load_dwordx4 v[52:55], v[2:3], off nt
	global_load_dwordx4 v[48:51], v[4:5], off nt
	v_ashrrev_i32_e32 v2, 31, v102
	v_mul_lo_u32 v4, s16, v2
	v_mul_lo_u32 v5, s17, v102
	v_mad_u64_u32 v[2:3], s[24:25], s16, v102, 0
	v_add3_u32 v3, v3, v4, v5
	v_ashrrev_i32_e32 v4, 31, v101
	v_mul_lo_u32 v6, s16, v4
	v_mul_lo_u32 v7, s17, v101
	v_mad_u64_u32 v[4:5], s[24:25], s16, v101, 0
	v_lshl_add_u64 v[2:3], v[2:3], 2, v[0:1]
	v_add3_u32 v5, v5, v6, v7
	v_lshl_add_u64 v[4:5], v[4:5], 2, v[0:1]
	global_load_dwordx4 v[44:47], v[2:3], off nt
	global_load_dwordx4 v[40:43], v[4:5], off nt
	v_ashrrev_i32_e32 v2, 31, v100
	v_mul_lo_u32 v4, s16, v2
	v_mul_lo_u32 v5, s17, v100
	v_mad_u64_u32 v[2:3], s[24:25], s16, v100, 0
	v_add3_u32 v3, v3, v4, v5
	v_ashrrev_i32_e32 v4, 31, v99
	v_mul_lo_u32 v6, s16, v4
	v_mul_lo_u32 v7, s17, v99
	v_mad_u64_u32 v[4:5], s[24:25], s16, v99, 0
	v_lshl_add_u64 v[2:3], v[2:3], 2, v[0:1]
	v_add3_u32 v5, v5, v6, v7
	v_lshl_add_u64 v[4:5], v[4:5], 2, v[0:1]
	global_load_dwordx4 v[36:39], v[2:3], off nt
	global_load_dwordx4 v[32:35], v[4:5], off nt
	v_ashrrev_i32_e32 v2, 31, v98
	v_mul_lo_u32 v4, s16, v2
	v_mul_lo_u32 v5, s17, v98
	v_mad_u64_u32 v[2:3], s[24:25], s16, v98, 0
	v_add3_u32 v3, v3, v4, v5
	v_ashrrev_i32_e32 v4, 31, v97
	v_mul_lo_u32 v6, s16, v4
	v_mul_lo_u32 v7, s17, v97
	v_mad_u64_u32 v[4:5], s[24:25], s16, v97, 0
	v_lshl_add_u64 v[2:3], v[2:3], 2, v[0:1]
	v_add3_u32 v5, v5, v6, v7
	v_lshl_add_u64 v[4:5], v[4:5], 2, v[0:1]
	global_load_dwordx4 v[28:31], v[2:3], off nt
	global_load_dwordx4 v[24:27], v[4:5], off nt
	v_ashrrev_i32_e32 v2, 31, v96
	v_mul_lo_u32 v4, s16, v2
	v_mul_lo_u32 v5, s17, v96
	v_mad_u64_u32 v[2:3], s[24:25], s16, v96, 0
	v_add3_u32 v3, v3, v4, v5
	v_ashrrev_i32_e32 v4, 31, v95
	v_mul_lo_u32 v6, s16, v4
	v_mul_lo_u32 v7, s17, v95
	v_mad_u64_u32 v[4:5], s[24:25], s16, v95, 0
	v_lshl_add_u64 v[2:3], v[2:3], 2, v[0:1]
	v_add3_u32 v5, v5, v6, v7
	v_lshl_add_u64 v[4:5], v[4:5], 2, v[0:1]
	global_load_dwordx4 v[20:23], v[2:3], off nt
	global_load_dwordx4 v[16:19], v[4:5], off nt
	v_ashrrev_i32_e32 v2, 31, v94
	v_mul_lo_u32 v4, s16, v2
	v_mul_lo_u32 v5, s17, v94
	v_mad_u64_u32 v[2:3], s[24:25], s16, v94, 0
	v_add3_u32 v3, v3, v4, v5
	v_ashrrev_i32_e32 v4, 31, v93
	v_mul_lo_u32 v6, s16, v4
	v_mul_lo_u32 v7, s17, v93
	v_mad_u64_u32 v[4:5], s[24:25], s16, v93, 0
	v_lshl_add_u64 v[2:3], v[2:3], 2, v[0:1]
	v_add3_u32 v5, v5, v6, v7
	v_lshl_add_u64 v[4:5], v[4:5], 2, v[0:1]
	global_load_dwordx4 v[12:15], v[2:3], off nt
	global_load_dwordx4 v[8:11], v[4:5], off nt
	v_ashrrev_i32_e32 v2, 31, v92
	v_mul_lo_u32 v4, s16, v2
	v_mul_lo_u32 v5, s17, v92
	v_mad_u64_u32 v[2:3], s[24:25], s16, v92, 0
	v_add3_u32 v3, v3, v4, v5
	v_ashrrev_i32_e32 v4, 31, v91
	v_mul_lo_u32 v6, s16, v4
	v_mul_lo_u32 v7, s17, v91
	v_mad_u64_u32 v[4:5], s[24:25], s16, v91, 0
	v_add3_u32 v5, v5, v6, v7
	v_lshl_add_u64 v[2:3], v[2:3], 2, v[0:1]
	v_lshl_add_u64 v[0:1], v[4:5], 2, v[0:1]
	global_load_dwordx4 v[4:7], v[2:3], off nt
	s_nop 0
	global_load_dwordx4 v[0:3], v[0:1], off nt
	s_or_b64 s[4:5], s[4:5], s[10:11]
	s_and_b64 vcc, exec, s[4:5]
	v_lshl_add_u64 v[72:73], v[70:71], 2, s[44:45]
	s_cbranch_vccnz .LBB0_183
; #define LAS __attribute__((address_space(3)))
; DI unsigned pk2(float lo, float hi) { const f32x2 v = {lo, hi}; return __builtin_bit_cast(unsigned, __builtin_convertvector(v, bf16x2_t)); }
; template <bool F8> DI void tr_tile(const float* __restrict__ W, int ldn, int K, int k0, int nsrc0, unsigned char* __restrict__ WT, int ndst0, LAS unsigned char* scr, int lane, float wscale, const float* gk = nullptr  ) {
;     ...
;     for (int i = 0; i < 16; ++i) { f32x4 x = F8 ? v[i] * wscale : v[i]; if (!F8 && gk) x = x * gk[k0 + 4 * i + r];
;         *(LAS unsigned long long*)(scr + (4 * i + r) * 144 + c4 * 8) = (unsigned long long)pk2(x[0], x[1]) | ((unsigned long long)pk2(x[2], x[3]) << 32); }
	s_waitcnt vmcnt(15)
	v_mov_b32_e32 v108, v206
	v_pk_mul_f32 v[62:63], v[62:63], v[108:109] op_sel_hi:[1,0]
	v_pk_mul_f32 v[60:61], v[60:61], v[108:109] op_sel_hi:[1,0]
.LBB0_183:
	s_xor_b64 s[24:25], s[4:5], -1
	s_waitcnt vmcnt(15)
	v_cvt_pk_bf16_f32 v108, v60, v61
	v_cndmask_b32_e64 v61, 0, 1, s[24:25]
	v_cvt_pk_bf16_f32 v109, v62, v63
	v_add_u32_e32 v60, v77, v78
	v_cmp_ne_u32_e64 s[4:5], 1, v61
	s_andn2_b64 vcc, exec, s[24:25]
	ds_write_b64 v60, v[108:109]
	s_cbranch_vccnz .LBB0_185
	s_waitcnt vmcnt(14)
	v_mov_b32_e32 v62, v207
	v_pk_mul_f32 v[58:59], v[58:59], v[62:63] op_sel_hi:[1,0]
	v_pk_mul_f32 v[56:57], v[56:57], v[62:63] op_sel_hi:[1,0]
.LBB0_185:
	s_waitcnt vmcnt(14)
	v_cvt_pk_bf16_f32 v56, v56, v57
	v_cvt_pk_bf16_f32 v57, v58, v59
	s_and_b64 vcc, exec, s[4:5]
	ds_write_b64 v60, v[56:57] offset:576
	s_cbranch_vccnz .LBB0_187
	s_waitcnt vmcnt(13)
	v_mov_b32_e32 v56, v208
	v_pk_mul_f32 v[54:55], v[54:55], v[56:57] op_sel_hi:[1,0]
	v_pk_mul_f32 v[52:53], v[52:53], v[56:57] op_sel_hi:[1,0]
.LBB0_187:
	s_waitcnt vmcnt(13)
	v_cvt_pk_bf16_f32 v52, v52, v53
	v_cvt_pk_bf16_f32 v53, v54, v55
	s_and_b64 vcc, exec, s[4:5]
	ds_write_b64 v60, v[52:53] offset:1152
	s_cbranch_vccnz .LBB0_189
	s_waitcnt vmcnt(12)
	v_mov_b32_e32 v52, v209
	v_pk_mul_f32 v[50:51], v[50:51], v[52:53] op_sel_hi:[1,0]
	v_pk_mul_f32 v[48:49], v[48:49], v[52:53] op_sel_hi:[1,0]
.LBB0_189:
	s_waitcnt vmcnt(12)
	v_cvt_pk_bf16_f32 v48, v48, v49
	v_cvt_pk_bf16_f32 v49, v50, v51
	s_and_b64 vcc, exec, s[4:5]
	ds_write_b64 v60, v[48:49] offset:1728
	s_cbranch_vccnz .LBB0_191
	s_waitcnt vmcnt(11)
	v_mov_b32_e32 v48, v210
	v_pk_mul_f32 v[46:47], v[46:47], v[48:49] op_sel_hi:[1,0]
	v_pk_mul_f32 v[44:45], v[44:45], v[48:49] op_sel_hi:[1,0]
.LBB0_191:
	s_waitcnt vmcnt(11)
	v_cvt_pk_bf16_f32 v44, v44, v45
	v_cvt_pk_bf16_f32 v45, v46, v47
	s_and_b64 vcc, exec, s[4:5]
	ds_write_b64 v60, v[44:45] offset:2304
	s_cbranch_vccnz .LBB0_193
	s_waitcnt vmcnt(10)
	v_mov_b32_e32 v44, v211
	v_pk_mul_f32 v[42:43], v[42:43], v[44:45] op_sel_hi:[1,0]
	v_pk_mul_f32 v[40:41], v[40:41], v[44:45] op_sel_hi:[1,0]
.LBB0_193:
	s_waitcnt vmcnt(10)
	v_cvt_pk_bf16_f32 v40, v40, v41
	v_cvt_pk_bf16_f32 v41, v42, v43
	s_and_b64 vcc, exec, s[4:5]
	ds_write_b64 v60, v[40:41] offset:2880
	s_cbranch_vccnz .LBB0_195
	s_waitcnt vmcnt(9)
	v_mov_b32_e32 v40, v212
	v_pk_mul_f32 v[38:39], v[38:39], v[40:41] op_sel_hi:[1,0]
	v_pk_mul_f32 v[36:37], v[36:37], v[40:41] op_sel_hi:[1,0]
.LBB0_195:
	s_waitcnt vmcnt(9)
	v_cvt_pk_bf16_f32 v36, v36, v37
	v_cvt_pk_bf16_f32 v37, v38, v39
	s_and_b64 vcc, exec, s[4:5]
	ds_write_b64 v60, v[36:37] offset:3456
	s_cbranch_vccnz .LBB0_197
	s_waitcnt vmcnt(8)
	v_mov_b32_e32 v36, v213
	v_pk_mul_f32 v[34:35], v[34:35], v[36:37] op_sel_hi:[1,0]
	v_pk_mul_f32 v[32:33], v[32:33], v[36:37] op_sel_hi:[1,0]
.LBB0_197:
	s_waitcnt vmcnt(8)
	v_cvt_pk_bf16_f32 v32, v32, v33
	v_cvt_pk_bf16_f32 v33, v34, v35
	s_and_b64 vcc, exec, s[4:5]
	ds_write_b64 v60, v[32:33] offset:4032
	s_cbranch_vccnz .LBB0_199
	s_waitcnt vmcnt(7)
	v_mov_b32_e32 v32, v214
	v_pk_mul_f32 v[30:31], v[30:31], v[32:33] op_sel_hi:[1,0]
	v_pk_mul_f32 v[28:29], v[28:29], v[32:33] op_sel_hi:[1,0]
.LBB0_199:
	s_waitcnt vmcnt(7)
	v_cvt_pk_bf16_f32 v28, v28, v29
	v_cvt_pk_bf16_f32 v29, v30, v31
	s_and_b64 vcc, exec, s[4:5]
	ds_write_b64 v60, v[28:29] offset:4608
	s_cbranch_vccnz .LBB0_201
	s_waitcnt vmcnt(6)
	v_mov_b32_e32 v28, v215
	v_pk_mul_f32 v[26:27], v[26:27], v[28:29] op_sel_hi:[1,0]
	v_pk_mul_f32 v[24:25], v[24:25], v[28:29] op_sel_hi:[1,0]
.LBB0_201:
	s_waitcnt vmcnt(6)
	v_cvt_pk_bf16_f32 v24, v24, v25
	v_cvt_pk_bf16_f32 v25, v26, v27
	s_and_b64 vcc, exec, s[4:5]
	ds_write_b64 v60, v[24:25] offset:5184
	s_cbranch_vccnz .LBB0_203
	s_waitcnt vmcnt(5)
	v_mov_b32_e32 v24, v216
	v_pk_mul_f32 v[22:23], v[22:23], v[24:25] op_sel_hi:[1,0]
	v_pk_mul_f32 v[20:21], v[20:21], v[24:25] op_sel_hi:[1,0]
.LBB0_203:
	s_waitcnt vmcnt(5)
	v_cvt_pk_bf16_f32 v20, v20, v21
	v_cvt_pk_bf16_f32 v21, v22, v23
	s_and_b64 vcc, exec, s[4:5]
	ds_write_b64 v60, v[20:21] offset:5760
	s_cbranch_vccnz .LBB0_205
	s_waitcnt vmcnt(4)
	v_mov_b32_e32 v20, v217
	v_pk_mul_f32 v[18:19], v[18:19], v[20:21] op_sel_hi:[1,0]
	v_pk_mul_f32 v[16:17], v[16:17], v[20:21] op_sel_hi:[1,0]
.LBB0_205:
	s_waitcnt vmcnt(4)
	v_cvt_pk_bf16_f32 v16, v16, v17
	v_cvt_pk_bf16_f32 v17, v18, v19
	s_and_b64 vcc, exec, s[4:5]
	ds_write_b64 v60, v[16:17] offset:6336
	s_cbranch_vccnz .LBB0_207
	s_waitcnt vmcnt(3)
	v_mov_b32_e32 v16, v218
	v_pk_mul_f32 v[14:15], v[14:15], v[16:17] op_sel_hi:[1,0]
	v_pk_mul_f32 v[12:13], v[12:13], v[16:17] op_sel_hi:[1,0]
.LBB0_207:
	s_waitcnt vmcnt(3)
	v_cvt_pk_bf16_f32 v12, v12, v13
	v_cvt_pk_bf16_f32 v13, v14, v15
	s_and_b64 vcc, exec, s[4:5]
	ds_write_b64 v60, v[12:13] offset:6912
	s_cbranch_vccnz .LBB0_209
	s_waitcnt vmcnt(2)
	v_mov_b32_e32 v12, v219
	v_pk_mul_f32 v[10:11], v[10:11], v[12:13] op_sel_hi:[1,0]
	v_pk_mul_f32 v[8:9], v[8:9], v[12:13] op_sel_hi:[1,0]
.LBB0_209:
	s_waitcnt vmcnt(2)
	v_cvt_pk_bf16_f32 v8, v8, v9
	v_cvt_pk_bf16_f32 v9, v10, v11
	s_and_b64 vcc, exec, s[4:5]
	ds_write_b64 v60, v[8:9] offset:7488
	s_cbranch_vccnz .LBB0_211
	s_waitcnt vmcnt(1)
	v_mov_b32_e32 v8, v220
	v_pk_mul_f32 v[6:7], v[6:7], v[8:9] op_sel_hi:[1,0]
	v_pk_mul_f32 v[4:5], v[4:5], v[8:9] op_sel_hi:[1,0]
.LBB0_211:
	s_waitcnt vmcnt(1)
	v_cvt_pk_bf16_f32 v4, v4, v5
	v_cvt_pk_bf16_f32 v5, v6, v7
	s_and_b64 vcc, exec, s[4:5]
	ds_write_b64 v60, v[4:5] offset:8064
	s_cbranch_vccnz .LBB0_213
	s_waitcnt vmcnt(0)
	v_mov_b32_e32 v4, v221
	v_pk_mul_f32 v[2:3], v[2:3], v[4:5] op_sel_hi:[1,0]
	v_pk_mul_f32 v[0:1], v[0:1], v[4:5] op_sel_hi:[1,0]

.LBB0_282:
	s_cmp_lt_u32 s3, 0x40001
	s_mov_b64 s[18:19], 0
	s_cselect_b64 s[20:21], -1, 0
	s_mov_b64 s[22:23], -1
	s_and_b64 vcc, exec, s[20:21]
	s_cbranch_vccnz .LBB0_279
	s_branch .LBB0_276
	s_nop 0
	s_nop 0
	s_nop 0
	s_nop 0
	s_nop 0
	s_nop 0
	s_nop 0
	s_nop 0
	s_nop 0
	s_nop 0
	s_nop 0
	s_nop 0
	s_nop 0
	s_nop 0
	s_nop 0
	s_nop 0
	s_nop 0
	s_nop 0
	s_nop 0
	s_nop 0
	s_nop 0
	s_nop 0
	s_nop 0
	s_nop 0
	s_nop 0
	s_nop 0
	s_nop 0
	s_nop 0
	s_nop 0
	s_nop 0
	s_nop 0
	s_nop 0
	s_nop 0
	s_nop 0
	s_nop 0
	s_nop 0
	s_nop 0
	s_nop 0
	s_nop 0
	s_nop 0
	s_nop 0
	s_nop 0
	s_nop 0
	s_nop 0
